# P1b gemm stream: per-unit accumulator zeroing (64 v_mov_b64) removed; first stage of each unit runs SrcC=0 copies of the two stage bodies
# speedup vs baseline: 1.0228x; 1.0053x over previous
;     __device__ __forceinline__ bool swapab(const Desc& d) const { const int wc = (otid() >> 6) & 3; return (d.nt == 2 && wc >= 2) || (d.nt >= 7); }
; template <class PH>
; __device__ __forceinline__ void gemm_stream(unsigned char* smem, PH& ph) {
;     ...
;         for (int m = 0; m < 8; ++m)
; #pragma unroll
;             for (int n = 0; n < 4; ++n) acc[m][n] = (f32x4){0.f, 0.f, 0.f, 0.f};
;         bool swp = false; if constexpr (ph_swap<PH>::value) swp = ph.swapab(d_cmp);
;         const bool wact = wr * 128 < ph.nrows(d_cmp);
;         if constexpr (PH::ROUND_SYNC) { if (cu > 0) ph.round_sync(cu); ++cu; }
;         const int n1 = PH::HAS_MID ? PH::MID_STAGE : cnk;
; #pragma unroll 1
;         for (int sidx = 0; sidx < n1; ++sidx) GS_STEP();
.LBB0_223:
	v_mov_b32_e32 v2, v0
	s_cmp_eq_u32 s14, 2
	v_and_b32_e32 v2, 0x80, v2
	s_cselect_b64 s[6:7], -1, 0
	s_cmp_lg_u32 s14, 2
	v_cmp_ne_u32_e32 vcc, 0, v2
	s_cselect_b64 s[24:25], -1, 0
	s_and_b64 s[4:5], s[6:7], vcc
	s_cmp_gt_i32 s14, 6
	v_mov_b32_e32 v68, v67
	v_mov_b32_e32 v69, v67
	s_cselect_b64 s[36:37], -1, 0
	v_mov_b32_e32 v66, v67
	s_nor_b64 s[26:27], s[36:37], s[4:5]
	s_mov_b32 s1, 0
	s_mov_b32 s4, s58
	s_branch .LBB0_226

.LBB0_248:
	s_cmp_eq_u32 s1, 0
	s_cbranch_scc1 .Lp1b_Z
	s_cmp_lg_u32 s26, 0
	s_cbranch_scc1 .Lp1b_XT
	s_and_b32 s5, s4, 0x10000
	v_or_b32_e32 v2, s5, v250
	v_xor_b32_e32 v6, 64, v2
	v_add_u32_e32 v68, s5, v249
	v_xor_b32_e32 v66, 64, v68
	ds_read_b128 v[26:29], v2 offset:0
	ds_read_b128 v[30:33], v6 offset:0
	ds_read_b128 v[18:21], v2 offset:2048
	ds_read_b128 v[22:25], v6 offset:2048
	ds_read_b128 v[10:13], v2 offset:4096
	ds_read_b128 v[14:17], v6 offset:4096
	ds_read_b128 v[2:5], v2 offset:6144
	ds_read_b128 v[6:9], v6 offset:6144
	ds_read_b128 v[58:61], v68 offset:0
	ds_read_b128 v[62:65], v66 offset:0
	ds_read_b128 v[42:45], v68 offset:2048
	ds_read_b128 v[46:49], v66 offset:2048
	ds_read_b128 v[50:53], v68 offset:4096
	ds_read_b128 v[54:57], v66 offset:4096
	ds_read_b128 v[34:37], v68 offset:6144
	ds_read_b128 v[38:41], v66 offset:6144
	s_waitcnt lgkmcnt(4)
	s_nop 0
	v_mfma_scale_f32_16x16x128_f8f6f4 v[194:197], v[58:65], v[26:33], v[194:197], v218, v218 op_sel_hi:[0,0,0]
	v_mfma_scale_f32_16x16x128_f8f6f4 v[190:193], v[58:65], v[18:25], v[190:193], v218, v218 op_sel_hi:[0,0,0]
	v_mfma_scale_f32_16x16x128_f8f6f4 v[186:189], v[58:65], v[10:17], v[186:189], v218, v218 op_sel_hi:[0,0,0]
	v_mfma_scale_f32_16x16x128_f8f6f4 v[182:185], v[58:65], v[2:9], v[182:185], v218, v218 op_sel_hi:[0,0,0]
	v_mfma_scale_f32_16x16x128_f8f6f4 v[178:181], v[42:49], v[26:33], v[178:181], v218, v218 op_sel_hi:[0,0,0]
	v_mfma_scale_f32_16x16x128_f8f6f4 v[174:177], v[42:49], v[18:25], v[174:177], v218, v218 op_sel_hi:[0,0,0]
	v_mfma_scale_f32_16x16x128_f8f6f4 v[170:173], v[42:49], v[10:17], v[170:173], v218, v218 op_sel_hi:[0,0,0]
	v_mfma_scale_f32_16x16x128_f8f6f4 v[166:169], v[42:49], v[2:9], v[166:169], v218, v218 op_sel_hi:[0,0,0]
	ds_read_b128 v[58:61], v68 offset:8192
	ds_read_b128 v[62:65], v66 offset:8192
	ds_read_b128 v[42:45], v68 offset:10240
	ds_read_b128 v[46:49], v66 offset:10240
	s_waitcnt lgkmcnt(4)
	v_mfma_scale_f32_16x16x128_f8f6f4 v[162:165], v[50:57], v[26:33], v[162:165], v218, v218 op_sel_hi:[0,0,0]
	v_mfma_scale_f32_16x16x128_f8f6f4 v[158:161], v[50:57], v[18:25], v[158:161], v218, v218 op_sel_hi:[0,0,0]
	v_mfma_scale_f32_16x16x128_f8f6f4 v[154:157], v[50:57], v[10:17], v[154:157], v218, v218 op_sel_hi:[0,0,0]
	v_mfma_scale_f32_16x16x128_f8f6f4 v[150:153], v[50:57], v[2:9], v[150:153], v218, v218 op_sel_hi:[0,0,0]
	v_mfma_scale_f32_16x16x128_f8f6f4 v[146:149], v[34:41], v[26:33], v[146:149], v218, v218 op_sel_hi:[0,0,0]
	v_mfma_scale_f32_16x16x128_f8f6f4 v[142:145], v[34:41], v[18:25], v[142:145], v218, v218 op_sel_hi:[0,0,0]
	v_mfma_scale_f32_16x16x128_f8f6f4 v[138:141], v[34:41], v[10:17], v[138:141], v218, v218 op_sel_hi:[0,0,0]
	v_mfma_scale_f32_16x16x128_f8f6f4 v[134:137], v[34:41], v[2:9], v[134:137], v218, v218 op_sel_hi:[0,0,0]
	ds_read_b128 v[50:53], v68 offset:12288
	ds_read_b128 v[54:57], v66 offset:12288
	ds_read_b128 v[34:37], v68 offset:14336
	ds_read_b128 v[38:41], v66 offset:14336
	s_waitcnt lgkmcnt(4)
	v_mfma_scale_f32_16x16x128_f8f6f4 v[130:133], v[58:65], v[26:33], v[130:133], v218, v218 op_sel_hi:[0,0,0]
	v_mfma_scale_f32_16x16x128_f8f6f4 v[126:129], v[58:65], v[18:25], v[126:129], v218, v218 op_sel_hi:[0,0,0]
	v_mfma_scale_f32_16x16x128_f8f6f4 v[122:125], v[58:65], v[10:17], v[122:125], v218, v218 op_sel_hi:[0,0,0]
	v_mfma_scale_f32_16x16x128_f8f6f4 v[118:121], v[58:65], v[2:9], v[118:121], v218, v218 op_sel_hi:[0,0,0]
	v_mfma_scale_f32_16x16x128_f8f6f4 v[114:117], v[42:49], v[26:33], v[114:117], v218, v218 op_sel_hi:[0,0,0]
	v_mfma_scale_f32_16x16x128_f8f6f4 v[110:113], v[42:49], v[18:25], v[110:113], v218, v218 op_sel_hi:[0,0,0]
	v_mfma_scale_f32_16x16x128_f8f6f4 v[106:109], v[42:49], v[10:17], v[106:109], v218, v218 op_sel_hi:[0,0,0]
	v_mfma_scale_f32_16x16x128_f8f6f4 v[102:105], v[42:49], v[2:9], v[102:105], v218, v218 op_sel_hi:[0,0,0]
	s_waitcnt lgkmcnt(0)
	v_mfma_scale_f32_16x16x128_f8f6f4 v[98:101], v[50:57], v[26:33], v[98:101], v218, v218 op_sel_hi:[0,0,0]
	v_mfma_scale_f32_16x16x128_f8f6f4 v[94:97], v[50:57], v[18:25], v[94:97], v218, v218 op_sel_hi:[0,0,0]
	v_mfma_scale_f32_16x16x128_f8f6f4 v[90:93], v[50:57], v[10:17], v[90:93], v218, v218 op_sel_hi:[0,0,0]
	v_mfma_scale_f32_16x16x128_f8f6f4 v[86:89], v[50:57], v[2:9], v[86:89], v218, v218 op_sel_hi:[0,0,0]
	v_mfma_scale_f32_16x16x128_f8f6f4 v[82:85], v[34:41], v[26:33], v[82:85], v218, v218 op_sel_hi:[0,0,0]
	v_mfma_scale_f32_16x16x128_f8f6f4 v[78:81], v[34:41], v[18:25], v[78:81], v218, v218 op_sel_hi:[0,0,0]
	v_mfma_scale_f32_16x16x128_f8f6f4 v[74:77], v[34:41], v[10:17], v[74:77], v218, v218 op_sel_hi:[0,0,0]
	v_mfma_scale_f32_16x16x128_f8f6f4 v[70:73], v[34:41], v[2:9], v[70:73], v218, v218 op_sel_hi:[0,0,0]
	s_branch .LBB0_225

.Lp1b_Z:
	s_cmp_lg_u32 s26, 0
	s_cbranch_scc1 .Lp1b_ZT
	s_and_b32 s5, s4, 0x10000
	v_or_b32_e32 v2, s5, v250
	v_xor_b32_e32 v6, 64, v2
	v_add_u32_e32 v68, s5, v249
	v_xor_b32_e32 v66, 64, v68
	ds_read_b128 v[26:29], v2 offset:0
	ds_read_b128 v[30:33], v6 offset:0
	ds_read_b128 v[18:21], v2 offset:2048
	ds_read_b128 v[22:25], v6 offset:2048
	ds_read_b128 v[10:13], v2 offset:4096
	ds_read_b128 v[14:17], v6 offset:4096
	ds_read_b128 v[2:5], v2 offset:6144
	ds_read_b128 v[6:9], v6 offset:6144
	ds_read_b128 v[58:61], v68 offset:0
	ds_read_b128 v[62:65], v66 offset:0
	ds_read_b128 v[42:45], v68 offset:2048
	ds_read_b128 v[46:49], v66 offset:2048
	ds_read_b128 v[50:53], v68 offset:4096
	ds_read_b128 v[54:57], v66 offset:4096
	ds_read_b128 v[34:37], v68 offset:6144
	ds_read_b128 v[38:41], v66 offset:6144
	s_waitcnt lgkmcnt(4)
	s_nop 0
	v_mfma_scale_f32_16x16x128_f8f6f4 v[194:197], v[58:65], v[26:33], 0, v218, v218 op_sel_hi:[0,0,0]
	v_mfma_scale_f32_16x16x128_f8f6f4 v[190:193], v[58:65], v[18:25], 0, v218, v218 op_sel_hi:[0,0,0]
	v_mfma_scale_f32_16x16x128_f8f6f4 v[186:189], v[58:65], v[10:17], 0, v218, v218 op_sel_hi:[0,0,0]
	v_mfma_scale_f32_16x16x128_f8f6f4 v[182:185], v[58:65], v[2:9], 0, v218, v218 op_sel_hi:[0,0,0]
	v_mfma_scale_f32_16x16x128_f8f6f4 v[178:181], v[42:49], v[26:33], 0, v218, v218 op_sel_hi:[0,0,0]
	v_mfma_scale_f32_16x16x128_f8f6f4 v[174:177], v[42:49], v[18:25], 0, v218, v218 op_sel_hi:[0,0,0]
	v_mfma_scale_f32_16x16x128_f8f6f4 v[170:173], v[42:49], v[10:17], 0, v218, v218 op_sel_hi:[0,0,0]
	v_mfma_scale_f32_16x16x128_f8f6f4 v[166:169], v[42:49], v[2:9], 0, v218, v218 op_sel_hi:[0,0,0]
	ds_read_b128 v[58:61], v68 offset:8192
	ds_read_b128 v[62:65], v66 offset:8192
	ds_read_b128 v[42:45], v68 offset:10240
	ds_read_b128 v[46:49], v66 offset:10240
	s_waitcnt lgkmcnt(4)
	v_mfma_scale_f32_16x16x128_f8f6f4 v[162:165], v[50:57], v[26:33], 0, v218, v218 op_sel_hi:[0,0,0]
	v_mfma_scale_f32_16x16x128_f8f6f4 v[158:161], v[50:57], v[18:25], 0, v218, v218 op_sel_hi:[0,0,0]
	v_mfma_scale_f32_16x16x128_f8f6f4 v[154:157], v[50:57], v[10:17], 0, v218, v218 op_sel_hi:[0,0,0]
	v_mfma_scale_f32_16x16x128_f8f6f4 v[150:153], v[50:57], v[2:9], 0, v218, v218 op_sel_hi:[0,0,0]
	v_mfma_scale_f32_16x16x128_f8f6f4 v[146:149], v[34:41], v[26:33], 0, v218, v218 op_sel_hi:[0,0,0]
	v_mfma_scale_f32_16x16x128_f8f6f4 v[142:145], v[34:41], v[18:25], 0, v218, v218 op_sel_hi:[0,0,0]
	v_mfma_scale_f32_16x16x128_f8f6f4 v[138:141], v[34:41], v[10:17], 0, v218, v218 op_sel_hi:[0,0,0]
	v_mfma_scale_f32_16x16x128_f8f6f4 v[134:137], v[34:41], v[2:9], 0, v218, v218 op_sel_hi:[0,0,0]
	ds_read_b128 v[50:53], v68 offset:12288
	ds_read_b128 v[54:57], v66 offset:12288
	ds_read_b128 v[34:37], v68 offset:14336
	ds_read_b128 v[38:41], v66 offset:14336
	s_waitcnt lgkmcnt(4)
	v_mfma_scale_f32_16x16x128_f8f6f4 v[130:133], v[58:65], v[26:33], 0, v218, v218 op_sel_hi:[0,0,0]
	v_mfma_scale_f32_16x16x128_f8f6f4 v[126:129], v[58:65], v[18:25], 0, v218, v218 op_sel_hi:[0,0,0]
	v_mfma_scale_f32_16x16x128_f8f6f4 v[122:125], v[58:65], v[10:17], 0, v218, v218 op_sel_hi:[0,0,0]
	v_mfma_scale_f32_16x16x128_f8f6f4 v[118:121], v[58:65], v[2:9], 0, v218, v218 op_sel_hi:[0,0,0]
	v_mfma_scale_f32_16x16x128_f8f6f4 v[114:117], v[42:49], v[26:33], 0, v218, v218 op_sel_hi:[0,0,0]
	v_mfma_scale_f32_16x16x128_f8f6f4 v[110:113], v[42:49], v[18:25], 0, v218, v218 op_sel_hi:[0,0,0]
	v_mfma_scale_f32_16x16x128_f8f6f4 v[106:109], v[42:49], v[10:17], 0, v218, v218 op_sel_hi:[0,0,0]
	v_mfma_scale_f32_16x16x128_f8f6f4 v[102:105], v[42:49], v[2:9], 0, v218, v218 op_sel_hi:[0,0,0]
	s_waitcnt lgkmcnt(0)
	v_mfma_scale_f32_16x16x128_f8f6f4 v[98:101], v[50:57], v[26:33], 0, v218, v218 op_sel_hi:[0,0,0]
	v_mfma_scale_f32_16x16x128_f8f6f4 v[94:97], v[50:57], v[18:25], 0, v218, v218 op_sel_hi:[0,0,0]
	v_mfma_scale_f32_16x16x128_f8f6f4 v[90:93], v[50:57], v[10:17], 0, v218, v218 op_sel_hi:[0,0,0]
	v_mfma_scale_f32_16x16x128_f8f6f4 v[86:89], v[50:57], v[2:9], 0, v218, v218 op_sel_hi:[0,0,0]
	v_mfma_scale_f32_16x16x128_f8f6f4 v[82:85], v[34:41], v[26:33], 0, v218, v218 op_sel_hi:[0,0,0]
	v_mfma_scale_f32_16x16x128_f8f6f4 v[78:81], v[34:41], v[18:25], 0, v218, v218 op_sel_hi:[0,0,0]
	v_mfma_scale_f32_16x16x128_f8f6f4 v[74:77], v[34:41], v[10:17], 0, v218, v218 op_sel_hi:[0,0,0]
	v_mfma_scale_f32_16x16x128_f8f6f4 v[70:73], v[34:41], v[2:9], 0, v218, v218 op_sel_hi:[0,0,0]
	s_branch .LBB0_225
.Lp1b_ZT:
	s_and_b32 s5, s4, 0x10000
	v_or_b32_e32 v2, s5, v250
	v_xor_b32_e32 v6, 64, v2
	v_add_u32_e32 v68, s5, v249
	v_xor_b32_e32 v66, 64, v68
	ds_read_b128 v[26:29], v2 offset:0
	ds_read_b128 v[30:33], v6 offset:0
	ds_read_b128 v[18:21], v2 offset:2048
	ds_read_b128 v[22:25], v6 offset:2048
	ds_read_b128 v[10:13], v2 offset:4096
	ds_read_b128 v[14:17], v6 offset:4096
	ds_read_b128 v[2:5], v2 offset:6144
	ds_read_b128 v[6:9], v6 offset:6144
	ds_read_b128 v[58:61], v68 offset:0
	ds_read_b128 v[62:65], v66 offset:0
	ds_read_b128 v[42:45], v68 offset:2048
	ds_read_b128 v[46:49], v66 offset:2048
	ds_read_b128 v[50:53], v68 offset:4096
	ds_read_b128 v[54:57], v66 offset:4096
	ds_read_b128 v[34:37], v68 offset:6144
	ds_read_b128 v[38:41], v66 offset:6144
	s_waitcnt lgkmcnt(4)
	s_nop 0
	v_mfma_scale_f32_16x16x128_f8f6f4 v[194:197], v[26:33], v[58:65], 0, v218, v218 op_sel_hi:[0,0,0]
	v_mfma_scale_f32_16x16x128_f8f6f4 v[190:193], v[18:25], v[58:65], 0, v218, v218 op_sel_hi:[0,0,0]
	v_mfma_scale_f32_16x16x128_f8f6f4 v[186:189], v[10:17], v[58:65], 0, v218, v218 op_sel_hi:[0,0,0]
	v_mfma_scale_f32_16x16x128_f8f6f4 v[182:185], v[2:9], v[58:65], 0, v218, v218 op_sel_hi:[0,0,0]
	v_mfma_scale_f32_16x16x128_f8f6f4 v[178:181], v[26:33], v[42:49], 0, v218, v218 op_sel_hi:[0,0,0]
	v_mfma_scale_f32_16x16x128_f8f6f4 v[174:177], v[18:25], v[42:49], 0, v218, v218 op_sel_hi:[0,0,0]
	v_mfma_scale_f32_16x16x128_f8f6f4 v[170:173], v[10:17], v[42:49], 0, v218, v218 op_sel_hi:[0,0,0]
	v_mfma_scale_f32_16x16x128_f8f6f4 v[166:169], v[2:9], v[42:49], 0, v218, v218 op_sel_hi:[0,0,0]
	ds_read_b128 v[58:61], v68 offset:8192
	ds_read_b128 v[62:65], v66 offset:8192
	ds_read_b128 v[42:45], v68 offset:10240
	ds_read_b128 v[46:49], v66 offset:10240
	s_waitcnt lgkmcnt(4)
	v_mfma_scale_f32_16x16x128_f8f6f4 v[162:165], v[26:33], v[50:57], 0, v218, v218 op_sel_hi:[0,0,0]
	v_mfma_scale_f32_16x16x128_f8f6f4 v[158:161], v[18:25], v[50:57], 0, v218, v218 op_sel_hi:[0,0,0]
	v_mfma_scale_f32_16x16x128_f8f6f4 v[154:157], v[10:17], v[50:57], 0, v218, v218 op_sel_hi:[0,0,0]
	v_mfma_scale_f32_16x16x128_f8f6f4 v[150:153], v[2:9], v[50:57], 0, v218, v218 op_sel_hi:[0,0,0]
	v_mfma_scale_f32_16x16x128_f8f6f4 v[146:149], v[26:33], v[34:41], 0, v218, v218 op_sel_hi:[0,0,0]
	v_mfma_scale_f32_16x16x128_f8f6f4 v[142:145], v[18:25], v[34:41], 0, v218, v218 op_sel_hi:[0,0,0]
	v_mfma_scale_f32_16x16x128_f8f6f4 v[138:141], v[10:17], v[34:41], 0, v218, v218 op_sel_hi:[0,0,0]
	v_mfma_scale_f32_16x16x128_f8f6f4 v[134:137], v[2:9], v[34:41], 0, v218, v218 op_sel_hi:[0,0,0]
	ds_read_b128 v[50:53], v68 offset:12288
	ds_read_b128 v[54:57], v66 offset:12288
	ds_read_b128 v[34:37], v68 offset:14336
	ds_read_b128 v[38:41], v66 offset:14336
	s_waitcnt lgkmcnt(4)
	v_mfma_scale_f32_16x16x128_f8f6f4 v[130:133], v[26:33], v[58:65], 0, v218, v218 op_sel_hi:[0,0,0]
	v_mfma_scale_f32_16x16x128_f8f6f4 v[126:129], v[18:25], v[58:65], 0, v218, v218 op_sel_hi:[0,0,0]
	v_mfma_scale_f32_16x16x128_f8f6f4 v[122:125], v[10:17], v[58:65], 0, v218, v218 op_sel_hi:[0,0,0]
	v_mfma_scale_f32_16x16x128_f8f6f4 v[118:121], v[2:9], v[58:65], 0, v218, v218 op_sel_hi:[0,0,0]
	v_mfma_scale_f32_16x16x128_f8f6f4 v[114:117], v[26:33], v[42:49], 0, v218, v218 op_sel_hi:[0,0,0]
	v_mfma_scale_f32_16x16x128_f8f6f4 v[110:113], v[18:25], v[42:49], 0, v218, v218 op_sel_hi:[0,0,0]
	v_mfma_scale_f32_16x16x128_f8f6f4 v[106:109], v[10:17], v[42:49], 0, v218, v218 op_sel_hi:[0,0,0]
	v_mfma_scale_f32_16x16x128_f8f6f4 v[102:105], v[2:9], v[42:49], 0, v218, v218 op_sel_hi:[0,0,0]
	s_waitcnt lgkmcnt(0)
	v_mfma_scale_f32_16x16x128_f8f6f4 v[98:101], v[26:33], v[50:57], 0, v218, v218 op_sel_hi:[0,0,0]
	v_mfma_scale_f32_16x16x128_f8f6f4 v[94:97], v[18:25], v[50:57], 0, v218, v218 op_sel_hi:[0,0,0]
	v_mfma_scale_f32_16x16x128_f8f6f4 v[90:93], v[10:17], v[50:57], 0, v218, v218 op_sel_hi:[0,0,0]
	v_mfma_scale_f32_16x16x128_f8f6f4 v[86:89], v[2:9], v[50:57], 0, v218, v218 op_sel_hi:[0,0,0]
	v_mfma_scale_f32_16x16x128_f8f6f4 v[82:85], v[26:33], v[34:41], 0, v218, v218 op_sel_hi:[0,0,0]
	v_mfma_scale_f32_16x16x128_f8f6f4 v[78:81], v[18:25], v[34:41], 0, v218, v218 op_sel_hi:[0,0,0]
	v_mfma_scale_f32_16x16x128_f8f6f4 v[74:77], v[10:17], v[34:41], 0, v218, v218 op_sel_hi:[0,0,0]
	v_mfma_scale_f32_16x16x128_f8f6f4 v[70:73], v[2:9], v[34:41], 0, v218, v218 op_sel_hi:[0,0,0]
	s_branch .LBB0_225
